# in-proj fp8 GEMM k-loop: phase-5 B-fragment LDS reads issued in the MFMA shadow of phase 4 (LDS reads balanced across phases)
# baseline (speedup 1.0000x reference)
; #define G8_STAGE2(bufoff, gbase, v0, v1) do { \
;         __builtin_amdgcn_global_load_lds((const unsigned*)((const char*)(gbase) + (v0)), (LAS unsigned*)(lds + (bufoff) + ldsw), 16, 0, 0); \
;         __builtin_amdgcn_global_load_lds((const unsigned*)((const char*)(gbase) + (v1)), (LAS unsigned*)(lds + (bufoff) + ldsw + 8192), 16, 0, 0); } while (0)
; #define G8_LDA(dst, b, h) do { _Pragma("unroll") for (int m = 0; m < 4; ++m) _Pragma("unroll") for (int k = 0; k < 2; ++k) dst[m][k] = *(const LAS bf16x8*)(lds + G8_SA(b, h) + aoff + m * 2048 + k * 1024); } while (0)
; #define G8_LDB(dst, b, h) do { _Pragma("unroll") for (int n = 0; n < 2; ++n) _Pragma("unroll") for (int k = 0; k < 2; ++k) dst[n][k] = *(const LAS bf16x8*)(lds + G8_SB(b, h) + boff + n * 2048 + k * 1024); } while (0)
; #define G8_WAIT_V(n) asm volatile("s_waitcnt vmcnt(" #n ")" ::: "memory")
; #define G8_WAIT_L(n) asm volatile("s_waitcnt lgkmcnt(" #n ")" ::: "memory")
; #define G8_BAR __builtin_amdgcn_s_barrier()
; #define G8_SCHED __builtin_amdgcn_sched_barrier(0)
; template <class Epi, class Sched, class Ops, bool FP8 = false>
; __device__ __forceinline__ void gemm_phase(LAS unsigned char* lds, const int RB, const Sched& S, const Ops& G, const Epi& E, const int wave_) {
;     ...
;             if (!sk0_) { G8_LDB(B0, 0, 0); G8_SCHED; G8_LDA(At, 0, 0); }
;             G8_STAGE2(G8_SA(1, 1), a1, c10, c11);
;             G8_WAIT_L(8); G8_BAR; G8_WAIT_L(0); if (!sk0_) G8_MMA(0, 0, At, B0);
;             G8_BAR; G8_SCHED;
;             if (!(sk0_ || hn_)) G8_LDB(B1, 0, 1);
;             G8_STAGE2(G8_SB(0, 0), b2, voffB[0], voffB[1]);
;             G8_BAR; G8_WAIT_L(0); if (!(sk0_ || hn_)) G8_MMA(0, 1, At, B1);
;             G8_BAR;
;             if (!hm_) G8_LDA(At, 0, 1);
;             G8_STAGE2(G8_SA(0, 0), a2, s00, s01);
;             G8_BAR; G8_WAIT_L(0); if (!hm_) G8_MMA(1, 0, At, B0);
;             G8_BAR; G8_SCHED;
;             G8_STAGE2(G8_SB(0, 1), b2 + hstep, voffB[0], voffB[1]);
;             G8_WAIT_V(6); G8_BAR; if (!(hm_ || hn_)) G8_MMA(1, 1, At, B1);
;             G8_BAR;
;             if (!sk0_) { G8_LDB(B0, 1, 0); G8_SCHED; G8_LDA(At, 1, 0); }
.LBB0_298:
	ds_read_b128 v[8:11], v184
	ds_read_b128 v[12:15], v184 offset:1024
	ds_read_b128 v[0:3], v184 offset:2048
	ds_read_b128 v[4:7], v184 offset:3072
	s_add_u32 s8, s6, 0x80
	s_addc_u32 s9, s7, 0
	s_cmp_eq_u32 s34, 12
	s_cselect_b32 s69, s0, s9
	s_cselect_b32 s68, s1, s8
	s_cselect_b32 s9, s14, s33
	s_cselect_b32 s8, s23, s27
	v_lshl_add_u64 v[168:169], s[6:7], 0, v[166:167]
	s_add_i32 m0, s61, 0xc000
	ds_read_b128 v[190:193], v185
	ds_read_b128 v[194:197], v185 offset:1024
	ds_read_b128 v[198:201], v185 offset:2048
	ds_read_b128 v[202:205], v185 offset:3072
	ds_read_b128 v[206:209], v185 offset:4096
	ds_read_b128 v[210:213], v185 offset:5120
	ds_read_b128 v[214:217], v185 offset:6144
	ds_read_b128 v[218:221], v185 offset:7168
	global_load_lds_dwordx4 v[168:169], off
	v_lshl_add_u64 v[168:169], s[6:7], 0, v[164:165]
	s_add_i32 m0, s61, 0xe000
	s_nop 0
	global_load_lds_dwordx4 v[168:169], off
	s_waitcnt lgkmcnt(8)
	s_barrier
	s_waitcnt lgkmcnt(0)
	s_setprio 1
	s_waitcnt lgkmcnt(0)
	v_mfma_f32_16x16x128_f8f6f4 v[140:143], v[8:15], v[190:197], v[140:143]
	v_mfma_f32_16x16x128_f8f6f4 v[136:139], v[0:7], v[190:197], v[136:139]
	v_mfma_f32_16x16x128_f8f6f4 v[132:135], v[8:15], v[198:205], v[132:135]
	v_mfma_f32_16x16x128_f8f6f4 v[128:131], v[0:7], v[198:205], v[128:131]
	v_mfma_f32_16x16x128_f8f6f4 v[124:127], v[8:15], v[206:213], v[124:127]
	v_mfma_f32_16x16x128_f8f6f4 v[120:123], v[0:7], v[206:213], v[120:123]
	v_mfma_f32_16x16x128_f8f6f4 v[116:119], v[8:15], v[214:221], v[116:119]
	v_mfma_f32_16x16x128_f8f6f4 v[112:115], v[0:7], v[214:221], v[112:115]
	s_setprio 0
	s_barrier
	s_add_i32 s35, s88, s54
	v_lshl_add_u64 v[168:169], s[8:9], 0, v[146:147]
	s_mov_b32 m0, s35
	ds_read_b128 v[222:225], v186
	ds_read_b128 v[226:229], v186 offset:1024
	ds_read_b128 v[230:233], v186 offset:2048
	ds_read_b128 v[234:237], v186 offset:3072
	global_load_lds_dwordx4 v[168:169], off
	v_lshl_add_u64 v[170:171], s[8:9], 0, v[144:145]
	s_add_i32 m0, s35, 0x2000
	s_nop 0
	global_load_lds_dwordx4 v[170:171], off
	s_barrier
	s_waitcnt lgkmcnt(0)
	s_setprio 1
	s_waitcnt lgkmcnt(0)
	v_mfma_f32_16x16x128_f8f6f4 v[84:87], v[222:229], v[190:197], v[84:87]
	v_mfma_f32_16x16x128_f8f6f4 v[76:79], v[230:237], v[190:197], v[76:79]
	v_mfma_f32_16x16x128_f8f6f4 v[68:71], v[222:229], v[198:205], v[68:71]
	v_mfma_f32_16x16x128_f8f6f4 v[64:67], v[230:237], v[198:205], v[64:67]
	v_mfma_f32_16x16x128_f8f6f4 v[60:63], v[222:229], v[206:213], v[60:63]
	v_mfma_f32_16x16x128_f8f6f4 v[56:59], v[230:237], v[206:213], v[56:59]
	v_mfma_f32_16x16x128_f8f6f4 v[52:55], v[222:229], v[214:221], v[52:55]
	v_mfma_f32_16x16x128_f8f6f4 v[48:51], v[230:237], v[214:221], v[48:51]
	s_setprio 0
	s_mov_b32 m0, s61
	v_lshl_add_u64 v[172:173], s[68:69], 0, v[148:149]
	s_barrier
	ds_read_b128 v[190:193], v185 offset:16384
	ds_read_b128 v[194:197], v185 offset:17408
	ds_read_b128 v[198:201], v185 offset:18432
	ds_read_b128 v[202:205], v185 offset:19456
	ds_read_b128 v[206:209], v185 offset:20480
	ds_read_b128 v[210:213], v185 offset:21504
	ds_read_b128 v[214:217], v185 offset:22528
	ds_read_b128 v[218:221], v185 offset:23552
	global_load_lds_dwordx4 v[172:173], off
	v_lshl_add_u64 v[174:175], s[68:69], 0, v[150:151]
	s_mov_b32 m0, s64
	s_nop 0
	global_load_lds_dwordx4 v[174:175], off
	s_barrier
	s_waitcnt lgkmcnt(0)
	s_setprio 1
	s_waitcnt lgkmcnt(0)
	v_mfma_f32_16x16x128_f8f6f4 v[108:111], v[8:15], v[190:197], v[108:111]
	v_mfma_f32_16x16x128_f8f6f4 v[104:107], v[0:7], v[190:197], v[104:107]
	v_mfma_f32_16x16x128_f8f6f4 v[100:103], v[8:15], v[198:205], v[100:103]
	v_mfma_f32_16x16x128_f8f6f4 v[96:99], v[0:7], v[198:205], v[96:99]
	v_mfma_f32_16x16x128_f8f6f4 v[92:95], v[8:15], v[206:213], v[92:95]
	v_mfma_f32_16x16x128_f8f6f4 v[88:91], v[0:7], v[206:213], v[88:91]
	v_mfma_f32_16x16x128_f8f6f4 v[80:83], v[8:15], v[214:221], v[80:83]
	v_mfma_f32_16x16x128_f8f6f4 v[72:75], v[0:7], v[214:221], v[72:75]
	s_setprio 0
	s_barrier
	s_add_u32 s36, s8, 0x40000
	s_addc_u32 s37, s9, 0
	s_add_i32 s35, s89, s54
	v_lshl_add_u64 v[0:1], s[36:37], 0, v[146:147]
	s_mov_b32 m0, s35
	s_nop 0
	global_load_lds_dwordx4 v[0:1], off
	v_lshl_add_u64 v[0:1], s[36:37], 0, v[144:145]
	s_add_i32 m0, s35, 0x2000
	s_nop 0
	global_load_lds_dwordx4 v[0:1], off
	s_waitcnt vmcnt(6)
	s_barrier
	s_setprio 1
	v_mfma_f32_16x16x128_f8f6f4 v[44:47], v[222:229], v[190:197], v[44:47]
	s_add_i32 s35, 0, 0x18000
	v_add_u32_e32 v12, s35, v179
	v_mfma_f32_16x16x128_f8f6f4 v[40:43], v[230:237], v[190:197], v[40:43]
	ds_read_b128 v[0:3], v12
	v_mfma_f32_16x16x128_f8f6f4 v[36:39], v[222:229], v[198:205], v[36:39]
	ds_read_b128 v[4:7], v12 offset:1024
	v_mfma_f32_16x16x128_f8f6f4 v[32:35], v[230:237], v[198:205], v[32:35]
	ds_read_b128 v[8:11], v12 offset:2048
	v_mfma_f32_16x16x128_f8f6f4 v[28:31], v[222:229], v[206:213], v[28:31]
	ds_read_b128 v[12:15], v12 offset:3072
	v_mfma_f32_16x16x128_f8f6f4 v[24:27], v[230:237], v[206:213], v[24:27]
	v_mfma_f32_16x16x128_f8f6f4 v[20:23], v[222:229], v[214:221], v[20:23]
	v_mfma_f32_16x16x128_f8f6f4 v[16:19], v[230:237], v[214:221], v[16:19]
	s_setprio 0
	s_barrier
	s_mov_b32 m0, s65
	v_lshl_add_u64 v[176:177], s[68:69], 0, v[152:153]
	ds_read_b128 v[190:193], v185 offset:32768
	ds_read_b128 v[194:197], v185 offset:33792
	ds_read_b128 v[198:201], v185 offset:34816
	ds_read_b128 v[202:205], v185 offset:35840
	ds_read_b128 v[206:209], v185 offset:36864
	ds_read_b128 v[210:213], v185 offset:37888
	ds_read_b128 v[214:217], v185 offset:38912
	ds_read_b128 v[218:221], v185 offset:39936
	global_load_lds_dwordx4 v[176:177], off
	v_lshl_add_u64 v[176:177], s[68:69], 0, v[154:155]
	s_mov_b32 m0, s66
	s_nop 0
	global_load_lds_dwordx4 v[176:177], off
	s_waitcnt lgkmcnt(8)
	s_barrier
; #define G8_STAGE2(bufoff, gbase, v0, v1) do { \
;         __builtin_amdgcn_global_load_lds((const unsigned*)((const char*)(gbase) + (v0)), (LAS unsigned*)(lds + (bufoff) + ldsw), 16, 0, 0); \
;         __builtin_amdgcn_global_load_lds((const unsigned*)((const char*)(gbase) + (v1)), (LAS unsigned*)(lds + (bufoff) + ldsw + 8192), 16, 0, 0); } while (0)
; #define G8_LDA(dst, b, h) do { _Pragma("unroll") for (int m = 0; m < 4; ++m) _Pragma("unroll") for (int k = 0; k < 2; ++k) dst[m][k] = *(const LAS bf16x8*)(lds + G8_SA(b, h) + aoff + m * 2048 + k * 1024); } while (0)
; #define G8_LDB(dst, b, h) do { _Pragma("unroll") for (int n = 0; n < 2; ++n) _Pragma("unroll") for (int k = 0; k < 2; ++k) dst[n][k] = *(const LAS bf16x8*)(lds + G8_SB(b, h) + boff + n * 2048 + k * 1024); } while (0)
; #define G8_WAIT_V(n) asm volatile("s_waitcnt vmcnt(" #n ")" ::: "memory")
; #define G8_WAIT_L(n) asm volatile("s_waitcnt lgkmcnt(" #n ")" ::: "memory")
; #define G8_BAR __builtin_amdgcn_s_barrier()
; #define G8_SCHED __builtin_amdgcn_sched_barrier(0)
; template <class Epi, class Sched, class Ops, bool FP8 = false>
; __device__ __forceinline__ void gemm_phase(LAS unsigned char* lds, const int RB, const Sched& S, const Ops& G, const Epi& E, const int wave_) {
;     ...
;             G8_WAIT_L(8); G8_BAR; G8_WAIT_L(0); if (!sk0_) G8_MMA(0, 0, At, B0);
;             G8_BAR; G8_SCHED;
;             if (!(sk0_ || hn_)) G8_LDB(B1, 1, 1);
;             G8_STAGE2(G8_SB(1, 0), b3, voffB[0], voffB[1]);
;             G8_BAR; G8_WAIT_L(0); if (!(sk0_ || hn_)) G8_MMA(0, 1, At, B1);
;             G8_BAR;
;             if (!hm_) G8_LDA(At, 1, 1);
;             G8_STAGE2(G8_SA(1, 0), a3, s00, s01);
;             G8_BAR; G8_WAIT_L(0); if (!hm_) G8_MMA(1, 0, At, B0);
;             G8_BAR; G8_SCHED;
;             G8_STAGE2(G8_SB(1, 1), b3 + hstep, voffB[0], voffB[1]);
;             G8_WAIT_V(6); G8_BAR; if (!(hm_ || hn_)) G8_MMA(1, 1, At, B1);
;             G8_BAR;
;         }
;         if constexpr (FP8) {
;             asm volatile("s_nop 15\n\ts_nop 15" ::: "memory");
	s_waitcnt lgkmcnt(0)
	s_setprio 1
	s_waitcnt lgkmcnt(0)
	v_mfma_f32_16x16x128_f8f6f4 v[140:143], v[0:7], v[190:197], v[140:143]
	v_mfma_f32_16x16x128_f8f6f4 v[136:139], v[8:15], v[190:197], v[136:139]
	v_mfma_f32_16x16x128_f8f6f4 v[132:135], v[0:7], v[198:205], v[132:135]
	v_mfma_f32_16x16x128_f8f6f4 v[128:131], v[8:15], v[198:205], v[128:131]
	v_mfma_f32_16x16x128_f8f6f4 v[124:127], v[0:7], v[206:213], v[124:127]
	v_mfma_f32_16x16x128_f8f6f4 v[120:123], v[8:15], v[206:213], v[120:123]
	v_mfma_f32_16x16x128_f8f6f4 v[116:119], v[0:7], v[214:221], v[116:119]
	v_mfma_f32_16x16x128_f8f6f4 v[112:115], v[8:15], v[214:221], v[112:115]
	s_setprio 0
	s_barrier
	s_add_i32 s36, 0, 0x1c000
	s_add_i32 s35, s35, s54
	v_add_u32_e32 v156, s36, v179
	v_lshl_add_u64 v[168:169], v[168:169], 0, s[16:17]
	s_mov_b32 m0, s35
	ds_read_b128 v[222:225], v156
	ds_read_b128 v[226:229], v156 offset:1024
	ds_read_b128 v[230:233], v156 offset:2048
	ds_read_b128 v[234:237], v156 offset:3072
	global_load_lds_dwordx4 v[168:169], off
	v_lshl_add_u64 v[168:169], v[170:171], 0, s[16:17]
	s_add_i32 m0, s35, 0x2000
	s_nop 0
	global_load_lds_dwordx4 v[168:169], off
	s_barrier
	s_waitcnt lgkmcnt(0)
	s_setprio 1
	s_waitcnt lgkmcnt(0)
	v_mfma_f32_16x16x128_f8f6f4 v[84:87], v[222:229], v[190:197], v[84:87]
	v_mfma_f32_16x16x128_f8f6f4 v[76:79], v[230:237], v[190:197], v[76:79]
	v_mfma_f32_16x16x128_f8f6f4 v[68:71], v[222:229], v[198:205], v[68:71]
	v_mfma_f32_16x16x128_f8f6f4 v[64:67], v[230:237], v[198:205], v[64:67]
	v_mfma_f32_16x16x128_f8f6f4 v[60:63], v[222:229], v[206:213], v[60:63]
	v_mfma_f32_16x16x128_f8f6f4 v[56:59], v[230:237], v[206:213], v[56:59]
	v_mfma_f32_16x16x128_f8f6f4 v[52:55], v[222:229], v[214:221], v[52:55]
	v_mfma_f32_16x16x128_f8f6f4 v[48:51], v[230:237], v[214:221], v[48:51]
	s_setprio 0
	s_mov_b32 m0, s84
	v_lshl_add_u64 v[168:169], v[172:173], 0, s[16:17]
	s_barrier
	ds_read_b128 v[190:193], v185 offset:49152
	ds_read_b128 v[194:197], v185 offset:50176
	ds_read_b128 v[198:201], v185 offset:51200
	ds_read_b128 v[202:205], v185 offset:52224
	ds_read_b128 v[206:209], v185 offset:53248
	ds_read_b128 v[210:213], v185 offset:54272
	ds_read_b128 v[214:217], v185 offset:55296
	ds_read_b128 v[218:221], v185 offset:56320
	global_load_lds_dwordx4 v[168:169], off
	v_lshl_add_u64 v[168:169], v[174:175], 0, s[16:17]
	s_mov_b32 m0, s85
	s_nop 0
	global_load_lds_dwordx4 v[168:169], off
	s_barrier
	s_waitcnt lgkmcnt(0)
	s_setprio 1
	s_waitcnt lgkmcnt(0)
	v_mfma_f32_16x16x128_f8f6f4 v[108:111], v[0:7], v[190:197], v[108:111]
	v_mfma_f32_16x16x128_f8f6f4 v[104:107], v[8:15], v[190:197], v[104:107]
	v_mfma_f32_16x16x128_f8f6f4 v[100:103], v[0:7], v[198:205], v[100:103]
	v_mfma_f32_16x16x128_f8f6f4 v[96:99], v[8:15], v[198:205], v[96:99]
	v_mfma_f32_16x16x128_f8f6f4 v[92:95], v[0:7], v[206:213], v[92:95]
	v_mfma_f32_16x16x128_f8f6f4 v[88:91], v[8:15], v[206:213], v[88:91]
	v_mfma_f32_16x16x128_f8f6f4 v[80:83], v[0:7], v[214:221], v[80:83]
	v_mfma_f32_16x16x128_f8f6f4 v[72:75], v[8:15], v[214:221], v[72:75]
	s_setprio 0
	s_barrier
	s_add_u32 s8, s8, 0x40080
	s_addc_u32 s9, s9, 0
	s_add_i32 s35, s36, s54
	v_lshl_add_u64 v[0:1], s[8:9], 0, v[146:147]
	s_mov_b32 m0, s35
	s_nop 0
	global_load_lds_dwordx4 v[0:1], off
	v_lshl_add_u64 v[0:1], s[8:9], 0, v[144:145]
	s_add_i32 m0, s35, 0x2000
	s_nop 0
	global_load_lds_dwordx4 v[0:1], off
	s_waitcnt vmcnt(6)
	s_barrier
	s_setprio 1
	v_mfma_f32_16x16x128_f8f6f4 v[44:47], v[222:229], v[190:197], v[44:47]
	v_mfma_f32_16x16x128_f8f6f4 v[40:43], v[230:237], v[190:197], v[40:43]
	v_mfma_f32_16x16x128_f8f6f4 v[36:39], v[222:229], v[198:205], v[36:39]
	v_mfma_f32_16x16x128_f8f6f4 v[32:35], v[230:237], v[198:205], v[32:35]
	v_mfma_f32_16x16x128_f8f6f4 v[28:31], v[222:229], v[206:213], v[28:31]
	v_mfma_f32_16x16x128_f8f6f4 v[24:27], v[230:237], v[206:213], v[24:27]
	v_mfma_f32_16x16x128_f8f6f4 v[20:23], v[222:229], v[214:221], v[20:23]
	v_mfma_f32_16x16x128_f8f6f4 v[16:19], v[230:237], v[214:221], v[16:19]
	s_setprio 0
	s_add_i32 s34, s34, 2
	s_add_u32 s6, s6, 0x100
	s_addc_u32 s7, s7, 0
	s_add_u32 s27, s27, 0x100
	s_addc_u32 s33, s33, 0
	s_cmp_gt_u32 s34, 13
	s_barrier
	s_cbranch_scc0 .LBB0_298
	s_nop 15
	s_nop 15
	s_lshl_b32 s23, s20, 8
	s_lshl_b32 s68, s70, 8
	s_add_i32 s23, s23, s55
	s_ashr_i32 s69, s68, 31
	s_sub_i32 s0, s70, 24
	v_or_b32_e32 v168, s23, v178
	v_lshl_add_u64 v[170:171], s[68:69], 2, v[160:161]
	s_cmp_gt_u32 s0, 9
	s_mov_b64 s[6:7], -1
	s_cbranch_scc0 .LBB0_373
	s_and_b32 s0, s70, -8
	s_cmp_lg_u32 s0, 16
	s_cbranch_scc0 .LBB0_306
	s_add_i32 s0, s68, 0xffffdc00
	s_ashr_i32 s1, s0, 31
	s_add_u32 s6, s62, s0
	s_addc_u32 s7, s63, s1
	s_cmp_gt_i32 s70, 23
	s_mov_b64 s[8:9], -1
	s_cbranch_scc0 .LBB0_303
	s_cmp_lt_u32 s70, 36
	s_cselect_b64 s[82:83], -1, 0
	s_cmp_gt_u32 s70, 35
	s_cselect_b64 s[80:81], -1, 0
	s_lshl_b64 s[0:1], s[68:69], 1
	v_readlane_b32 s8, v255, 4
	s_add_u32 s0, s8, s0
	v_readlane_b32 s8, v255, 5
	s_addc_u32 s1, s8, s1
	s_add_u32 s8, s0, 0xffffbc00
	s_addc_u32 s9, s1, -1
	s_and_b64 s[0:1], s[82:83], exec
	v_readlane_b32 s0, v254, 62
	v_readlane_b32 s1, v254, 63
	s_cselect_b32 s14, 0x200, 0
	s_cselect_b32 s87, s9, s1
	s_cselect_b32 s86, s8, s0
	s_mov_b64 s[8:9], 0
	s_mov_b64 s[78:79], s[14:15]
